# P8: 4-buffer A-half-0 LDS ring (two extra 16K buffers), K loop unrolled x2, 4 DMAs per load segment, all stages >= 4 intervals of flight
# baseline (speedup 1.0000x reference)
.LBB0_930:
	v_readlane_b32 s10, v254, 0
	v_readlane_b32 s11, v254, 1
	s_load_dwordx2 s[10:11], s[10:11], 0xa0
	s_mov_b64 s[12:13], 0x80
	v_lshl_add_u64 v[6:7], v[6:7], 0, s[12:13]
	s_waitcnt vmcnt(2)
	s_barrier
	s_waitcnt lgkmcnt(0)
	s_add_u32 s10, s10, 0x55400000
	s_addc_u32 s11, s11, 0
	s_add_i32 s51, s33, 0x18000
	s_lshl_b32 s5, s94, 12
	s_mov_b32 m0, s51
	s_add_i32 s52, s33, 0x1a000
	s_lshl_b32 s16, s4, 13
	s_and_b32 s5, s5, 0x3000
	global_load_lds_dwordx4 v[6:7], off
	v_lshl_add_u64 v[4:5], v[4:5], 0, s[12:13]
	s_mov_b32 m0, s52
	s_add_i32 s53, s33, 0x8000
	s_add_i32 s54, s33, 0xa000
	global_load_lds_dwordx4 v[4:5], off
	v_lshl_add_u64 v[0:1], v[0:1], 0, s[12:13]
	s_mov_b32 m0, s53
	s_add_u32 s14, s40, 0x80080
	global_load_lds_dwordx4 v[0:1], off
	v_lshl_add_u64 v[0:1], v[2:3], 0, s[12:13]
	s_mov_b32 m0, s54
	s_addc_u32 s15, s41, 0
	s_add_i32 s55, s33, 0x1c000
	global_load_lds_dwordx4 v[0:1], off
	v_lshl_add_u64 v[0:1], s[14:15], 0, v[162:163]
	s_mov_b32 m0, s55
	s_add_i32 s56, s33, 0x1e000
	global_load_lds_dwordx4 v[0:1], off
	v_lshl_add_u64 v[0:1], s[14:15], 0, v[166:167]
	s_mov_b32 m0, s56
	v_lshlrev_b32_e32 v4, 2, v14
	global_load_lds_dwordx4 v[0:1], off
	v_lshrrev_b32_e32 v0, 1, v14
	v_and_b32_e32 v1, 15, v14
	v_and_b32_e32 v0, 24, v0
	v_lshlrev_b32_e32 v2, 1, v0
	v_lshlrev_b32_e32 v3, 6, v1
	v_and_b32_e32 v4, 32, v4
	s_add_i32 s5, s5, 0
	v_bitop3_b32 v2, v3, v4, v2 bitop3:0x36
	s_cmpk_lt_u32 s65, 0x100
	v_lshl_or_b32 v188, s4, 6, v1
	v_add_u32_e32 v3, s5, v2
	s_cselect_b64 s[14:15], -1, 0
	s_lshl_b64 s[4:5], s[94:95], 9
	s_ashr_i32 s57, s64, 31
	s_ashr_i32 s58, s68, 31
	v_readlane_b32 s18, v254, 14
	v_readlane_b32 s19, v254, 15
	s_add_u32 s4, s18, s4
	v_lshlrev_b32_e32 v168, 5, v1
	s_addc_u32 s5, s19, s5
	v_add_u32_e32 v4, 0, v2
	v_mov_b32_e32 v1, v169
	v_add_u32_e32 v189, 0x10000, v3
	v_add_u32_e32 v190, 0x10400, v3
	v_add_u32_e32 v191, 0x10800, v3
	v_add_u32_e32 v192, 0x10c00, v3
	v_add_u32_e32 v193, 0x14000, v3
	v_add_u32_e32 v194, 0x14400, v3
	v_add_u32_e32 v195, 0x14800, v3
	v_add_u32_e32 v196, 0x14c00, v3
	v_add_u32_e32 v197, 0x18000, v3
	v_add_u32_e32 v198, 0x18400, v3
	v_add_u32_e32 v199, 0x18800, v3
	v_add_u32_e32 v200, 0x18c00, v3
	v_add_u32_e32 v201, 0x1c000, v3
	v_add_u32_e32 v202, 0x1c400, v3
	v_add_u32_e32 v203, 0x1c800, v3
	v_add_u32_e32 v204, 0x1cc00, v3
	v_lshl_add_u64 v[2:3], s[4:5], 0, v[168:169]
	v_lshl_add_u64 v[170:171], v[2:3], 0, v[0:1]
	v_lshlrev_b32_e32 v0, 15, v8
	v_and_b32_e32 v0, 0xffff0000, v0
	v_lshl_add_u32 v0, v9, 12, v0
	v_and_b32_e32 v1, 1, v8
	v_lshl_or_b32 v0, v1, 6, v0
	v_lshl_add_u32 v172, v10, 1, v0
	v_lshlrev_b32_e32 v0, 15, v11
	v_and_b32_e32 v0, 0xffff0000, v0
	s_waitcnt vmcnt(6)
	v_lshl_add_u32 v0, v12, 12, v0
	v_and_b32_e32 v1, 1, v11
	v_lshl_or_b32 v0, v1, 6, v0
	v_mov_b32_e32 v173, v169
	v_lshl_add_u32 v174, v13, 1, v0
	v_mov_b32_e32 v175, v169
	v_mov_b64_e32 v[176:177], 0x1000
	v_mov_b64_e32 v[178:179], 0xfff
	v_add_u32_e32 v205, s16, v4
	s_mov_b32 s59, 0xffffff
	s_mov_b64 s[16:17], 0x10000
	s_mov_b64 s[18:19], 0x12000
	s_mov_b64 s[20:21], 0x14000
	s_mov_b64 s[22:23], 0x16000
	v_mov_b32_e32 v206, 2
	s_barrier
	v_readlane_b32 s82, v254, 10
	s_nop 3
	v_mov_b32_e32 v208, s82
	ds_read_b64 v[208:209], v208
	s_waitcnt lgkmcnt(0)
	s_nop 0
	v_readfirstlane_b32 s82, v208
	v_readfirstlane_b32 s83, v209
	s_mov_b32 s74, -1
	s_branch .LBB0_933

.LBB0_939:
	s_ashr_i32 s27, s26, 31
	s_lshl_b64 s[28:29], s[26:27], 20
	s_add_u32 s28, s0, s28
	s_addc_u32 s29, s1, s29
	s_and_b64 s[30:31], s[4:5], exec
	s_cselect_b32 s27, s29, s39
	s_cselect_b32 s35, s28, s38
	s_ashr_i32 s25, s24, 31
	s_lshl_b64 s[30:31], s[24:25], 20
	s_add_u32 s30, s2, s30
	s_addc_u32 s31, s3, s31
	s_and_b64 s[42:43], s[4:5], exec
	s_cselect_b32 s25, s31, s41
	s_cselect_b32 s37, s30, s40
	s_add_u32 s38, s38, 0x80080
	s_addc_u32 s39, s39, 0
	s_add_u32 s60, s40, 0x100
	v_mov_b32_e32 v32, 0
	s_mov_b32 s66, s64
	s_addc_u32 s61, s41, 0
	s_mov_b32 s64, -2
	v_mov_b32_e32 v33, v32
	v_mov_b32_e32 v34, v32
	v_mov_b32_e32 v35, v32
	v_mov_b32_e32 v36, v32
	v_mov_b32_e32 v37, v32
	v_mov_b32_e32 v38, v32
	v_mov_b32_e32 v39, v32
	v_mov_b32_e32 v48, v32
	v_mov_b32_e32 v49, v32
	v_mov_b32_e32 v50, v32
	v_mov_b32_e32 v51, v32
	v_mov_b32_e32 v52, v32
	v_mov_b32_e32 v53, v32
	v_mov_b32_e32 v54, v32
	v_mov_b32_e32 v55, v32
	v_mov_b32_e32 v64, v32
	v_mov_b32_e32 v65, v32
	v_mov_b32_e32 v66, v32
	v_mov_b32_e32 v67, v32
	v_mov_b32_e32 v68, v32
	v_mov_b32_e32 v69, v32
	v_mov_b32_e32 v70, v32
	v_mov_b32_e32 v71, v32
	v_mov_b32_e32 v80, v32
	v_mov_b32_e32 v81, v32
	v_mov_b32_e32 v82, v32
	v_mov_b32_e32 v83, v32
	v_mov_b32_e32 v84, v32
	v_mov_b32_e32 v85, v32
	v_mov_b32_e32 v86, v32
	v_mov_b32_e32 v87, v32
	v_mov_b32_e32 v40, v32
	v_mov_b32_e32 v41, v32
	v_mov_b32_e32 v42, v32
	v_mov_b32_e32 v43, v32
	v_mov_b32_e32 v44, v32
	v_mov_b32_e32 v45, v32
	v_mov_b32_e32 v46, v32
	v_mov_b32_e32 v47, v32
	v_mov_b32_e32 v56, v32
	v_mov_b32_e32 v57, v32
	v_mov_b32_e32 v58, v32
	v_mov_b32_e32 v59, v32
	v_mov_b32_e32 v60, v32
	v_mov_b32_e32 v61, v32
	v_mov_b32_e32 v62, v32
	v_mov_b32_e32 v63, v32
	v_mov_b32_e32 v72, v32
	v_mov_b32_e32 v73, v32
	v_mov_b32_e32 v74, v32
	v_mov_b32_e32 v75, v32
	v_mov_b32_e32 v76, v32
	v_mov_b32_e32 v77, v32
	v_mov_b32_e32 v78, v32
	v_mov_b32_e32 v79, v32
	v_mov_b32_e32 v88, v32
	v_mov_b32_e32 v89, v32
	v_mov_b32_e32 v90, v32
	v_mov_b32_e32 v91, v32
	v_mov_b32_e32 v92, v32
	v_mov_b32_e32 v93, v32
	v_mov_b32_e32 v94, v32
	v_mov_b32_e32 v95, v32
	v_mov_b32_e32 v96, v32
	v_mov_b32_e32 v97, v32
	v_mov_b32_e32 v98, v32
	v_mov_b32_e32 v99, v32
	v_mov_b32_e32 v100, v32
	v_mov_b32_e32 v101, v32
	v_mov_b32_e32 v102, v32
	v_mov_b32_e32 v103, v32
	v_mov_b32_e32 v112, v32
	v_mov_b32_e32 v113, v32
	v_mov_b32_e32 v114, v32
	v_mov_b32_e32 v115, v32
	v_mov_b32_e32 v116, v32
	v_mov_b32_e32 v117, v32
	v_mov_b32_e32 v118, v32
	v_mov_b32_e32 v119, v32
	v_mov_b32_e32 v128, v32
	v_mov_b32_e32 v129, v32
	v_mov_b32_e32 v130, v32
	v_mov_b32_e32 v131, v32
	v_mov_b32_e32 v132, v32
	v_mov_b32_e32 v133, v32
	v_mov_b32_e32 v134, v32
	v_mov_b32_e32 v135, v32
	v_mov_b32_e32 v144, v32
	v_mov_b32_e32 v145, v32
	v_mov_b32_e32 v146, v32
	v_mov_b32_e32 v147, v32
	v_mov_b32_e32 v148, v32
	v_mov_b32_e32 v149, v32
	v_mov_b32_e32 v150, v32
	v_mov_b32_e32 v151, v32
	v_mov_b32_e32 v104, v32
	v_mov_b32_e32 v105, v32
	v_mov_b32_e32 v106, v32
	v_mov_b32_e32 v107, v32
	v_mov_b32_e32 v108, v32
	v_mov_b32_e32 v109, v32
	v_mov_b32_e32 v110, v32
	v_mov_b32_e32 v111, v32
	v_mov_b32_e32 v120, v32
	v_mov_b32_e32 v121, v32
	v_mov_b32_e32 v122, v32
	v_mov_b32_e32 v123, v32
	v_mov_b32_e32 v124, v32
	v_mov_b32_e32 v125, v32
	v_mov_b32_e32 v126, v32
	v_mov_b32_e32 v127, v32
	v_mov_b32_e32 v136, v32
	v_mov_b32_e32 v137, v32
	v_mov_b32_e32 v138, v32
	v_mov_b32_e32 v139, v32
	v_mov_b32_e32 v140, v32
	v_mov_b32_e32 v141, v32
	v_mov_b32_e32 v142, v32
	v_mov_b32_e32 v143, v32
	v_mov_b32_e32 v152, v32
	v_mov_b32_e32 v153, v32
	v_mov_b32_e32 v154, v32
	v_mov_b32_e32 v155, v32
	v_mov_b32_e32 v156, v32
	v_mov_b32_e32 v157, v32
	v_mov_b32_e32 v158, v32
	v_mov_b32_e32 v159, v32
	v_add_u32_e32 v240, 0x20000, v205
	s_add_i32 s84, s33, 0x20000
	s_add_i32 s85, s33, 0x22000
	s_add_i32 s86, s33, 0x24000
	s_add_i32 s87, s33, 0x26000
.LBB0_940:
	ds_read_b128 v[16:19], v189
	ds_read_b128 v[20:23], v190
	ds_read_b128 v[24:27], v191
	ds_read_b128 v[28:31], v192
	ds_read_b128 v[0:3], v193
	ds_read_b128 v[4:7], v194
	ds_read_b128 v[8:11], v195
	ds_read_b128 v[12:15], v196
	s_add_u32 s40, s38, 0xfff80080
	s_addc_u32 s41, s39, -1
	s_cmp_eq_u32 s64, 28
	s_cselect_b32 s43, s27, s41
	s_cselect_b32 s42, s35, s40
	s_cselect_b32 s41, s25, s61
	s_cselect_b32 s40, s37, s60
	ds_read_b128 v[180:183], v205
	ds_read_b128 v[184:187], v205 offset:1024
	ds_read_b128 v[208:211], v205 offset:2048
	ds_read_b128 v[212:215], v205 offset:3072
	ds_read_b128 v[216:219], v205 offset:4096
	ds_read_b128 v[220:223], v205 offset:5120
	ds_read_b128 v[224:227], v205 offset:6144
	ds_read_b128 v[228:231], v205 offset:7168
	s_mov_b32 m0, s84
	s_nop 0
	global_load_lds_dwordx4 v160, s[42:43]
	s_mov_b32 m0, s85
	s_nop 0
	global_load_lds_dwordx4 v164, s[42:43]
	s_add_i32 m0, s33, 0xc000
	s_nop 0
	global_load_lds_dwordx4 v172, s[38:39]
	s_add_i32 m0, s33, 0xe000
	s_nop 0
	global_load_lds_dwordx4 v174, s[38:39]
	s_waitcnt vmcnt(8)
	s_waitcnt lgkmcnt(0)
	s_barrier
	s_setprio 1
	s_waitcnt lgkmcnt(0)
	s_bitcmp1_b32 s74, 0
	s_cbranch_scc0 .Lp8ra_0
	v_mfma_f32_16x16x128_f8f6f4 v[156:159], v[16:23], v[180:187], v[156:159]

.Lp8ra_15:
	s_setprio 0
	s_barrier
	s_add_u32 s62, s40, 0x80000
	ds_read_b128 v[208:211], v205 offset:16384
	ds_read_b128 v[212:215], v205 offset:17408
	ds_read_b128 v[216:219], v205 offset:18432
	ds_read_b128 v[220:223], v205 offset:19456
	ds_read_b128 v[224:227], v205 offset:20480
	ds_read_b128 v[228:231], v205 offset:21504
	ds_read_b128 v[232:235], v205 offset:22528
	ds_read_b128 v[236:239], v205 offset:23552
	s_addc_u32 s63, s41, 0
	s_mov_b32 m0, s44
	s_nop 0
	global_load_lds_dwordx4 v162, s[40:41]
	s_mov_b32 m0, s45
	s_nop 0
	global_load_lds_dwordx4 v166, s[40:41]
	s_mov_b32 m0, s46
	s_nop 0
	global_load_lds_dwordx4 v162, s[62:63]
	s_mov_b32 m0, s47
	s_nop 0
	global_load_lds_dwordx4 v166, s[62:63]
	s_waitcnt vmcnt(8)
	s_waitcnt lgkmcnt(0)
	s_barrier
	s_setprio 1
	s_waitcnt lgkmcnt(0)
	s_bitcmp1_b32 s74, 16
	s_cbranch_scc0 .Lp8ra_16
	v_mfma_f32_16x16x128_f8f6f4 v[92:95], v[16:23], v[208:215], v[92:95]

.Lp8ra_31:
	s_setprio 0
	s_barrier
	ds_read_b128 v[0:3], v197
	ds_read_b128 v[4:7], v198
	ds_read_b128 v[8:11], v199
	ds_read_b128 v[12:15], v200
	ds_read_b128 v[16:19], v201
	ds_read_b128 v[20:23], v202
	ds_read_b128 v[24:27], v203
	ds_read_b128 v[28:31], v204
	s_add_u32 s42, s42, 0x80000
	s_addc_u32 s43, s43, 0
	ds_read_b128 v[208:211], v205 offset:32768
	ds_read_b128 v[212:215], v205 offset:33792
	ds_read_b128 v[216:219], v205 offset:34816
	ds_read_b128 v[220:223], v205 offset:35840
	ds_read_b128 v[224:227], v205 offset:36864
	ds_read_b128 v[228:231], v205 offset:37888
	ds_read_b128 v[232:235], v205 offset:38912
	ds_read_b128 v[236:239], v205 offset:39936
	s_add_u32 s76, s42, 0xfff80080
	s_addc_u32 s77, s43, -1
	s_mov_b32 m0, s86
	s_nop 0
	global_load_lds_dwordx4 v160, s[76:77]
	s_mov_b32 m0, s87
	s_nop 0
	global_load_lds_dwordx4 v164, s[76:77]
	s_mov_b32 m0, s49
	s_nop 0
	global_load_lds_dwordx4 v160, s[42:43]
	s_mov_b32 m0, s50
	s_nop 0
	global_load_lds_dwordx4 v164, s[42:43]
	s_waitcnt vmcnt(8)
	s_waitcnt lgkmcnt(0)
	s_barrier
	s_setprio 1
	s_waitcnt lgkmcnt(0)
	s_bitcmp1_b32 s74, 0
	s_cbranch_scc0 .Lp8ra_32
	v_mfma_f32_16x16x128_f8f6f4 v[156:159], v[0:7], v[208:215], v[156:159]

.Lp8ra_47:
	s_setprio 0
	s_barrier
	s_add_u32 s40, s40, 0x80080
	ds_read_b128 v[208:211], v205 offset:49152
	ds_read_b128 v[212:215], v205 offset:50176
	ds_read_b128 v[216:219], v205 offset:51200
	ds_read_b128 v[220:223], v205 offset:52224
	ds_read_b128 v[224:227], v205 offset:53248
	ds_read_b128 v[228:231], v205 offset:54272
	ds_read_b128 v[232:235], v205 offset:55296
	ds_read_b128 v[236:239], v205 offset:56320
	s_addc_u32 s41, s41, 0
	s_add_u32 s76, s40, 0xfff80000
	s_addc_u32 s77, s41, -1
	s_mov_b32 m0, s51
	s_nop 0
	global_load_lds_dwordx4 v162, s[76:77]
	s_mov_b32 m0, s52
	s_nop 0
	global_load_lds_dwordx4 v166, s[76:77]
	s_mov_b32 m0, s55
	s_nop 0
	global_load_lds_dwordx4 v162, s[40:41]
	s_mov_b32 m0, s56
	s_nop 0
	global_load_lds_dwordx4 v166, s[40:41]
	s_waitcnt vmcnt(8)
	s_waitcnt lgkmcnt(0)
	s_barrier
	s_setprio 1
	s_waitcnt lgkmcnt(0)
	s_bitcmp1_b32 s74, 16
	s_cbranch_scc0 .Lp8ra_48
	v_mfma_f32_16x16x128_f8f6f4 v[92:95], v[0:7], v[208:215], v[92:95]

.Lp8r_bodyB:
	ds_read_b128 v[16:19], v189
	ds_read_b128 v[20:23], v190
	ds_read_b128 v[24:27], v191
	ds_read_b128 v[28:31], v192
	ds_read_b128 v[0:3], v193
	ds_read_b128 v[4:7], v194
	ds_read_b128 v[8:11], v195
	ds_read_b128 v[12:15], v196
	s_add_u32 s40, s38, 0xfff80080
	s_addc_u32 s41, s39, -1
	s_cmp_eq_u32 s64, 28
	s_cselect_b32 s43, s27, s41
	s_cselect_b32 s42, s35, s40
	s_cselect_b32 s41, s25, s61
	s_cselect_b32 s40, s37, s60
	ds_read_b128 v[180:183], v240
	ds_read_b128 v[184:187], v240 offset:1024
	ds_read_b128 v[208:211], v240 offset:2048
	ds_read_b128 v[212:215], v240 offset:3072
	ds_read_b128 v[216:219], v240 offset:4096
	ds_read_b128 v[220:223], v240 offset:5120
	ds_read_b128 v[224:227], v240 offset:6144
	ds_read_b128 v[228:231], v240 offset:7168
	s_mov_b32 m0, s33
	s_nop 0
	global_load_lds_dwordx4 v160, s[42:43]
	s_mov_b32 m0, s48
	s_nop 0
	global_load_lds_dwordx4 v164, s[42:43]
	s_add_i32 m0, s33, 0xc000
	s_nop 0
	global_load_lds_dwordx4 v172, s[38:39]
	s_add_i32 m0, s33, 0xe000
	s_nop 0
	global_load_lds_dwordx4 v174, s[38:39]
	s_waitcnt vmcnt(8)
	s_waitcnt lgkmcnt(0)
	s_barrier
	s_setprio 1
	s_waitcnt lgkmcnt(0)
	s_bitcmp1_b32 s74, 0
	s_cbranch_scc0 .Lp8rb_0
	v_mfma_f32_16x16x128_f8f6f4 v[156:159], v[16:23], v[180:187], v[156:159]

.Lp8rb_31:
	s_setprio 0
	s_barrier
	ds_read_b128 v[0:3], v197
	ds_read_b128 v[4:7], v198
	ds_read_b128 v[8:11], v199
	ds_read_b128 v[12:15], v200
	ds_read_b128 v[16:19], v201
	ds_read_b128 v[20:23], v202
	ds_read_b128 v[24:27], v203
	ds_read_b128 v[28:31], v204
	s_add_u32 s42, s42, 0x80000
	s_addc_u32 s43, s43, 0
	ds_read_b128 v[208:211], v240 offset:16384
	ds_read_b128 v[212:215], v240 offset:17408
	ds_read_b128 v[216:219], v240 offset:18432
	ds_read_b128 v[220:223], v240 offset:19456
	ds_read_b128 v[224:227], v240 offset:20480
	ds_read_b128 v[228:231], v240 offset:21504
	ds_read_b128 v[232:235], v240 offset:22528
	ds_read_b128 v[236:239], v240 offset:23552
	s_add_u32 s76, s42, 0xfff80080
	s_addc_u32 s77, s43, -1
	s_mov_b32 m0, s53
	s_nop 0
	global_load_lds_dwordx4 v160, s[76:77]
	s_mov_b32 m0, s54
	s_nop 0
	global_load_lds_dwordx4 v164, s[76:77]
	s_mov_b32 m0, s49
	s_nop 0
	global_load_lds_dwordx4 v160, s[42:43]
	s_mov_b32 m0, s50
	s_nop 0
	global_load_lds_dwordx4 v164, s[42:43]
	s_waitcnt vmcnt(8)
	s_waitcnt lgkmcnt(0)
	s_barrier
	s_setprio 1
	s_waitcnt lgkmcnt(0)
	s_bitcmp1_b32 s74, 0
	s_cbranch_scc0 .Lp8rb_32
	v_mfma_f32_16x16x128_f8f6f4 v[156:159], v[0:7], v[208:215], v[156:159]

.LBB0_1218:
	s_waitcnt vmcnt(0)
	s_barrier
	v_readlane_b32 s76, v254, 10
	s_nop 3
	v_mov_b32_e32 v0, s76
	v_mov_b32_e32 v2, s82
	v_mov_b32_e32 v3, s83
	ds_write_b64 v0, v[2:3]
	s_waitcnt lgkmcnt(0)
